# speedup vs baseline: 1.0114x; 1.0114x over previous
_Z6k_attnPKDF16_PKfPDF16_:
	s_load_dwordx4 s[4:7], s[0:1], 0x0
	s_load_dwordx2 s[8:9], s[0:1], 0x10
	s_lshr_b32 s0, s2, 3
	s_sub_i32 s0, 0x2ff, s0
	s_lshl_b32 s1, s2, 5
	s_mul_hi_i32 s2, s0, 0x2aaaaaab
	s_lshr_b32 s3, s2, 31
	s_ashr_i32 s2, s2, 2
	s_and_b32 s1, s1, 0xe0
	s_add_i32 s2, s2, s3
	s_add_i32 s1, s2, s1
	s_mul_i32 s2, s2, 24
	s_sub_i32 s0, s0, s2
	s_mul_i32 s2, s0, 43
	s_bfe_u32 s3, s2, 0x1000f
	s_bfe_u32 s2, s2, 0x80008
	s_add_i32 s2, s2, s3
	s_sext_i32_i8 s2, s2
	s_mul_i32 s3, s2, -6
	s_add_i32 s3, s3, s0
	s_lshl_b32 s0, s1, 2
	s_add_i32 s2, s0, s2
	s_mul_i32 s1, s2, 0x48000
	s_mul_hi_i32 s0, s2, 0x48000
	s_waitcnt lgkmcnt(0)
	s_add_u32 s4, s4, s1
	s_addc_u32 s5, s5, s0
	s_lshl_b32 s0, s3, 7
	s_ashr_i32 s1, s0, 31
	s_lshl_b64 s[0:1], s[0:1], 1
	s_add_u32 s4, s4, s0
	v_lshlrev_b32_e32 v2, 4, v0
	v_lshrrev_b32_e32 v9, 4, v0
	s_addc_u32 s5, s5, s1
	v_and_b32_e32 v2, 0xf0, v2
	v_mov_b32_e32 v3, 0
	v_mul_u32_u24_e32 v6, 0x900, v9
	v_lshl_add_u64 v[4:5], s[4:5], 0, v[2:3]
	v_lshlrev_b32_e32 v6, 1, v6
	v_mov_b32_e32 v7, v3
	v_lshl_add_u64 v[6:7], v[4:5], 0, v[6:7]
	global_load_dwordx4 v[10:13], v[6:7], off offset:1536 nt
	global_load_dwordx4 v[14:17], v[6:7], off offset:3072 nt
	v_or_b32_e32 v6, 0x100, v0
	v_lshrrev_b32_e32 v50, 4, v6
	v_mul_u32_u24_e32 v6, 0x900, v50
	v_lshlrev_b32_e32 v6, 1, v6
	v_mov_b32_e32 v7, v3
	v_lshl_add_u64 v[6:7], v[4:5], 0, v[6:7]
	global_load_dwordx4 v[18:21], v[6:7], off offset:1536 nt
	global_load_dwordx4 v[22:25], v[6:7], off offset:3072 nt
	v_or_b32_e32 v6, 0x200, v0
	v_lshrrev_b32_e32 v51, 4, v6
	v_mul_u32_u24_e32 v6, 0x900, v51
	v_lshlrev_b32_e32 v6, 1, v6
	v_mov_b32_e32 v7, v3
	v_lshl_add_u64 v[6:7], v[4:5], 0, v[6:7]
	global_load_dwordx4 v[26:29], v[6:7], off offset:1536 nt
	global_load_dwordx4 v[30:33], v[6:7], off offset:3072 nt
	v_or_b32_e32 v6, 0x300, v0
	v_lshrrev_b32_e32 v52, 4, v6
	v_mul_u32_u24_e32 v6, 0x900, v52
	v_lshlrev_b32_e32 v6, 1, v6
	v_mov_b32_e32 v7, v3
	v_lshrrev_b32_e32 v1, 6, v0
	v_lshl_add_u64 v[4:5], v[4:5], 0, v[6:7]
	v_and_b32_e32 v8, 15, v0
	global_load_dwordx4 v[34:37], v[4:5], off offset:1536 nt
	global_load_dwordx4 v[38:41], v[4:5], off offset:3072 nt
	v_lshlrev_b32_e32 v6, 4, v1
	v_or_b32_e32 v4, v6, v8
	v_mul_u32_u24_e32 v4, 0x900, v4
	v_lshlrev_b32_e32 v4, 1, v4
	v_mov_b32_e32 v5, v3
	v_lshl_add_u64 v[4:5], s[4:5], 0, v[4:5]
	v_and_b32_e32 v58, 48, v0
	v_mov_b32_e32 v59, v3
	v_lshl_add_u64 v[4:5], v[4:5], 0, v[58:59]
	global_load_dwordx4 v[42:45], v[4:5], off nt
	global_load_dwordx4 v[46:49], v[4:5], off offset:64 nt
	s_movk_i32 s3, 0x110
	s_movk_i32 s4, 0x120
	v_or_b32_e32 v7, 0x4800, v2
	v_mad_u32_u24 v59, v9, s4, v2
	v_mad_u32_u24 v9, v9, s3, v7
	v_mad_u32_u24 v60, v50, s4, v2
	v_mad_u32_u24 v61, v51, s4, v2
	v_mad_u32_u24 v62, v52, s4, v2
	v_mad_u32_u24 v63, v50, s3, v7
	v_mad_u32_u24 v64, v51, s3, v7
	v_mad_u32_u24 v7, v52, s3, v7
	global_load_dwordx4 v[50:53], v[4:5], off offset:128 nt
	global_load_dwordx4 v[54:57], v[4:5], off offset:192 nt
	v_lshlrev_b32_e32 v4, 2, v8
	v_mov_b32_e32 v5, v3
	v_lshl_add_u64 v[4:5], s[6:7], 0, v[4:5]
	s_movk_i32 s4, 0x900
	s_waitcnt vmcnt(11)
	ds_write_b128 v9, v[10:13]
	s_waitcnt vmcnt(10)
	ds_write_b128 v59, v[14:17]
	s_waitcnt vmcnt(9)
	ds_write_b128 v63, v[18:21]
	s_waitcnt vmcnt(8)
	ds_write_b128 v60, v[22:25]
	s_waitcnt vmcnt(7)
	ds_write_b128 v64, v[26:29]
	s_waitcnt vmcnt(6)
	ds_write_b128 v61, v[30:33]
	s_waitcnt vmcnt(5)
	ds_write_b128 v7, v[34:37]
	s_waitcnt vmcnt(4)
	ds_write_b128 v62, v[38:41]
	v_mad_u32_u24 v30, v8, s3, v58
	s_waitcnt lgkmcnt(0)
	s_barrier
	ds_read_b128 v[10:13], v30 offset:18432
	ds_read_b128 v[14:17], v30 offset:18496
	s_waitcnt vmcnt(3) lgkmcnt(1)
	v_mfma_f32_16x16x32_f16 a[0:3], v[42:45], v[10:13], 0
	v_bfe_u32 v7, v0, 4, 2
	v_lshlrev_b32_e32 v9, 2, v7
	v_mbcnt_lo_u32_b32 v39, -1, 0
	s_waitcnt vmcnt(2) lgkmcnt(0)
	v_mfma_f32_16x16x32_f16 a[0:3], v[46:49], v[14:17], a[0:3]
	ds_read_b128 v[10:13], v30 offset:22784
	ds_read_b128 v[14:17], v30 offset:22848
	s_waitcnt lgkmcnt(1)
	v_mfma_f32_16x16x32_f16 a[4:7], v[42:45], v[10:13], 0
	s_waitcnt lgkmcnt(0)
	v_mfma_f32_16x16x32_f16 a[4:7], v[46:49], v[14:17], a[4:7]
	ds_read_b128 v[10:13], v30 offset:27136
	ds_read_b128 v[14:17], v30 offset:27200
	s_waitcnt lgkmcnt(1)
	v_mfma_f32_16x16x32_f16 a[8:11], v[42:45], v[10:13], 0
	ds_read_b128 v[10:13], v30 offset:31488
	s_waitcnt lgkmcnt(1)
	v_mfma_f32_16x16x32_f16 a[8:11], v[46:49], v[14:17], a[8:11]
	ds_read_b128 v[14:17], v30 offset:31552
	s_waitcnt lgkmcnt(1)
	v_mfma_f32_16x16x32_f16 a[12:15], v[42:45], v[10:13], 0
	v_or_b32_e32 v10, v9, v6
	v_lshlrev_b32_e32 v10, 8, v10
	v_mov_b32_e32 v11, v3
	v_lshl_add_u64 v[4:5], v[4:5], 0, v[10:11]
	global_load_dword v31, v[4:5], off
	global_load_dword v32, v[4:5], off offset:64
	global_load_dword v33, v[4:5], off offset:128
	global_load_dword v34, v[4:5], off offset:192
	s_waitcnt lgkmcnt(0)
	v_mfma_f32_16x16x32_f16 a[12:15], v[46:49], v[14:17], a[12:15]
	ds_read_b128 v[10:13], v30 offset:18560
	ds_read_b128 v[14:17], v30 offset:18624
	ds_read_b128 v[18:21], v30 offset:22912
	s_waitcnt vmcnt(5) lgkmcnt(2)
	v_mfma_f32_16x16x32_f16 a[0:3], v[50:53], v[10:13], a[0:3]
	ds_read_b128 v[10:13], v30 offset:22976
	ds_read_b128 v[22:25], v30 offset:27264
	ds_read_b128 v[26:29], v30 offset:27328
	global_load_dword v35, v[4:5], off offset:256
	global_load_dword v36, v[4:5], off offset:320
	global_load_dword v37, v[4:5], off offset:384
	global_load_dword v38, v[4:5], off offset:448
	s_waitcnt lgkmcnt(3)
	v_mfma_f32_16x16x32_f16 a[4:7], v[50:53], v[18:21], a[4:7]
	ds_read_b128 v[18:21], v30 offset:31616
	s_waitcnt lgkmcnt(2)
	v_mfma_f32_16x16x32_f16 a[8:11], v[50:53], v[22:25], a[8:11]
	ds_read_b128 v[22:25], v30 offset:31680
	s_waitcnt lgkmcnt(1)
	v_mfma_f32_16x16x32_f16 a[12:15], v[50:53], v[18:21], a[12:15]
	v_mbcnt_hi_u32_b32 v19, -1, v39
	v_lshlrev_b32_e32 v20, 3, v7
	v_lshlrev_b32_e32 v18, 3, v0
	s_waitcnt vmcnt(8)
	v_mfma_f32_16x16x32_f16 a[8:11], v[54:57], v[26:29], a[8:11]
	v_bfe_u32 v0, v0, 2, 2
	v_or_b32_e32 v0, v9, v0
	v_mul_u32_u24_e32 v0, 0x120, v0
	s_waitcnt lgkmcnt(0)
	v_mfma_f32_16x16x32_f16 a[12:15], v[54:57], v[22:25], a[12:15]
	v_and_or_b32 v0, v18, 24, v0
	v_mfma_f32_16x16x32_f16 a[0:3], v[54:57], v[14:17], a[0:3]
	v_and_b32_e32 v15, 64, v19
	v_xor_b32_e32 v14, 1, v19
	v_accvgpr_read_b32 v17, a8
	v_mfma_f32_16x16x32_f16 a[4:7], v[54:57], v[10:13], a[4:7]
	v_add_u32_e32 v12, 64, v15
	v_cmp_lt_i32_e32 vcc, v14, v12
	v_accvgpr_read_b32 v21, a12
	v_xor_b32_e32 v16, 2, v19
	v_cndmask_b32_e32 v13, v19, v14, vcc
	v_accvgpr_read_b32 v14, a0
	v_lshlrev_b32_e32 v13, 2, v13
	v_cmp_lt_i32_e32 vcc, v16, v12
	v_accvgpr_read_b32 v15, a4
	v_xor_b32_e32 v10, 4, v19
	v_cndmask_b32_e32 v16, v19, v16, vcc
	v_lshlrev_b32_e32 v16, 2, v16
	v_xor_b32_e32 v11, 8, v19
	v_cmp_lt_i32_e32 vcc, v10, v12
	v_accvgpr_read_b32 v26, a9
	v_accvgpr_read_b32 v22, a1
	v_cndmask_b32_e32 v10, v19, v10, vcc
	v_cmp_lt_i32_e32 vcc, v11, v12
	v_lshlrev_b32_e32 v10, 2, v10
	v_accvgpr_read_b32 v25, a5
	v_cndmask_b32_e32 v11, v19, v11, vcc
	v_lshlrev_b32_e32 v11, 2, v11
	v_accvgpr_read_b32 v41, a14
	v_accvgpr_read_b32 v23, a2
	v_accvgpr_read_b32 v42, a15
	v_accvgpr_read_b32 v24, a3
	s_waitcnt vmcnt(7)
	v_fmac_f32_e32 v31, 0x3e0293ee, v14
	s_waitcnt vmcnt(6)
	v_fmac_f32_e32 v32, 0x3e0293ee, v15
	s_waitcnt vmcnt(5)
	v_fmac_f32_e32 v33, 0x3e0293ee, v17
	s_waitcnt vmcnt(4)
	v_fmac_f32_e32 v34, 0x3e0293ee, v21
	v_max_f32_e32 v14, v33, v34
	v_max3_f32 v14, v31, v32, v14
	s_nop 1
	v_mov_b32_dpp v15, v14 quad_perm:[1,0,3,2] row_mask:0xf bank_mask:0xf
	s_waitcnt vmcnt(3)
	v_fmac_f32_e32 v35, 0x3e0293ee, v22
	s_waitcnt vmcnt(2)
	v_fmac_f32_e32 v36, 0x3e0293ee, v25
	s_waitcnt vmcnt(1)
	v_fmac_f32_e32 v37, 0x3e0293ee, v26
	s_waitcnt lgkmcnt(0)
	v_max_f32_e32 v15, v15, v15
	v_max_f32_e32 v14, v14, v15
	s_nop 1
	v_mov_b32_dpp v15, v14 quad_perm:[2,3,0,1] row_mask:0xf bank_mask:0xf
	s_waitcnt lgkmcnt(0)
	v_max_f32_e32 v12, v15, v15
	global_load_dword v15, v[4:5], off offset:512
	global_load_dword v17, v[4:5], off offset:576
	global_load_dword v19, v[4:5], off offset:640
	global_load_dword v21, v[4:5], off offset:704
	v_max_f32_e32 v12, v14, v12
	s_nop 1
	v_mov_b32_dpp v14, v12 row_half_mirror row_mask:0xf bank_mask:0xf
	s_waitcnt lgkmcnt(0)
	v_max_f32_e32 v14, v14, v14
	v_max_f32_e32 v12, v12, v14
	s_nop 1
	v_mov_b32_dpp v14, v12 row_mirror row_mask:0xf bank_mask:0xf
	s_waitcnt lgkmcnt(0)
	v_max_f32_e32 v14, v14, v14
	v_max_f32_e32 v12, v12, v14
	v_sub_f32_e32 v14, v31, v12
	v_sub_f32_e32 v27, v32, v12
	v_sub_f32_e32 v28, v33, v12
	v_sub_f32_e32 v12, v34, v12
	global_load_dword v33, v[4:5], off offset:768
	global_load_dword v34, v[4:5], off offset:832
	global_load_dword v39, v[4:5], off offset:896
	global_load_dword v40, v[4:5], off offset:960
	v_exp_f32_e32 v14, v14
	v_exp_f32_e32 v27, v27
	v_exp_f32_e32 v28, v28
	v_exp_f32_e32 v12, v12
	v_add_f32_e32 v29, 0, v14
	v_add_f32_e32 v29, v29, v27
	v_add_f32_e32 v29, v29, v28
	v_add_f32_e32 v29, v29, v12
	s_nop 1
	v_mov_b32_dpp v30, v29 quad_perm:[1,0,3,2] row_mask:0xf bank_mask:0xf
	v_accvgpr_read_b32 v31, a13
	s_waitcnt vmcnt(8)
	v_fmac_f32_e32 v38, 0x3e0293ee, v31
	v_max_f32_e32 v26, v37, v38
	v_max3_f32 v26, v35, v36, v26
	s_waitcnt lgkmcnt(0)
	v_add_f32_e32 v22, v29, v30
	s_nop 1
	v_mov_b32_dpp v29, v26 quad_perm:[1,0,3,2] row_mask:0xf bank_mask:0xf
	v_accvgpr_read_b32 v32, a10
	s_nop 1
	v_mov_b32_dpp v25, v22 quad_perm:[2,3,0,1] row_mask:0xf bank_mask:0xf
	v_accvgpr_read_b32 v30, a6
	v_accvgpr_read_b32 v4, a11
	s_waitcnt lgkmcnt(1)
	v_max_f32_e32 v29, v29, v29
	v_max_f32_e32 v26, v26, v29
	s_nop 1
	v_mov_b32_dpp v29, v26 quad_perm:[2,3,0,1] row_mask:0xf bank_mask:0xf
	s_waitcnt lgkmcnt(1)
	v_add_f32_e32 v22, v22, v25
	s_nop 1
	v_mov_b32_dpp v25, v22 row_half_mirror row_mask:0xf bank_mask:0xf
	v_accvgpr_read_b32 v31, a7
	v_cvt_f16_f32_e32 v14, v14
	s_waitcnt lgkmcnt(1)
	v_max_f32_e32 v5, v29, v29
	v_max_f32_e32 v5, v26, v5
	s_nop 1
	v_mov_b32_dpp v26, v5 row_half_mirror row_mask:0xf bank_mask:0xf
	s_waitcnt lgkmcnt(1)
	v_add_f32_e32 v22, v22, v25
	s_nop 1
	v_mov_b32_dpp v25, v22 row_mirror row_mask:0xf bank_mask:0xf
	v_cvt_f16_f32_e32 v27, v27
	v_cvt_f16_f32_e32 v28, v28
	s_waitcnt lgkmcnt(1)
	v_max_f32_e32 v26, v26, v26
	v_max_f32_e32 v5, v5, v26
	s_nop 1
	v_mov_b32_dpp v26, v5 row_mirror row_mask:0xf bank_mask:0xf
	s_waitcnt lgkmcnt(1)
	v_add_f32_e32 v22, v22, v25
	v_div_scale_f32 v25, s[6:7], v22, v22, 1.0
	v_rcp_f32_e32 v29, v25
	s_waitcnt lgkmcnt(0)
	v_max_f32_e32 v26, v26, v26
	v_max_f32_e32 v5, v5, v26
	v_sub_f32_e32 v26, v35, v5
	v_fma_f32 v43, -v25, v29, 1.0
	v_exp_f32_e32 v26, v26
	v_sub_f32_e32 v35, v36, v5
	v_fmac_f32_e32 v29, v43, v29
	v_exp_f32_e32 v35, v35
	v_sub_f32_e32 v36, v37, v5
	v_exp_f32_e32 v36, v36
	v_sub_f32_e32 v5, v38, v5
	v_exp_f32_e32 v5, v5
	v_add_f32_e32 v37, 0, v26
	v_add_f32_e32 v37, v37, v35
	v_add_f32_e32 v37, v37, v36
	v_add_f32_e32 v37, v37, v5
	s_waitcnt vmcnt(7)
	v_fmac_f32_e32 v15, 0x3e0293ee, v23
	s_waitcnt vmcnt(6)
	v_fmac_f32_e32 v17, 0x3e0293ee, v30
	s_waitcnt vmcnt(5)
	v_fmac_f32_e32 v19, 0x3e0293ee, v32
	s_waitcnt vmcnt(4)
	v_fmac_f32_e32 v21, 0x3e0293ee, v41
	v_max_f32_e32 v23, v19, v21
	v_max3_f32 v23, v15, v17, v23
	s_nop 1
	v_mov_b32_dpp v30, v23 quad_perm:[1,0,3,2] row_mask:0xf bank_mask:0xf
	v_div_scale_f32 v32, vcc, 1.0, v22, 1.0
	v_mul_f32_e32 v41, v32, v29
	v_fma_f32 v43, -v25, v41, v32
	s_waitcnt lgkmcnt(0)
	v_max_f32_e32 v30, v30, v30
	v_max_f32_e32 v23, v23, v30
	s_nop 1
	v_mov_b32_dpp v30, v23 quad_perm:[2,3,0,1] row_mask:0xf bank_mask:0xf
	v_fmac_f32_e32 v41, v43, v29
	v_fma_f32 v25, -v25, v41, v32
	v_div_fmas_f32 v25, v25, v29, v41
	s_nop 1
	v_mov_b32_dpp v38, v37 quad_perm:[1,0,3,2] row_mask:0xf bank_mask:0xf
	s_waitcnt lgkmcnt(1)
	v_max_f32_e32 v30, v30, v30
	v_max_f32_e32 v23, v23, v30
	s_nop 1
	v_mov_b32_dpp v30, v23 row_half_mirror row_mask:0xf bank_mask:0xf
	s_waitcnt vmcnt(3)
	v_fmac_f32_e32 v33, 0x3e0293ee, v24
	s_waitcnt vmcnt(1)
	v_fmac_f32_e32 v39, 0x3e0293ee, v4
	s_waitcnt vmcnt(0)
	v_fmac_f32_e32 v40, 0x3e0293ee, v42
	v_fmac_f32_e32 v34, 0x3e0293ee, v31
	s_waitcnt lgkmcnt(0)
	v_max_f32_e32 v30, v30, v30
	v_max_f32_e32 v23, v23, v30
	s_nop 1
	v_mov_b32_dpp v30, v23 row_mirror row_mask:0xf bank_mask:0xf
	v_max_f32_e32 v4, v39, v40
	v_max3_f32 v4, v33, v34, v4
	v_add_f32_e32 v37, v37, v38
	s_nop 1
	v_mov_b32_dpp v38, v37 quad_perm:[2,3,0,1] row_mask:0xf bank_mask:0xf
	s_waitcnt lgkmcnt(1)
	v_max_f32_e32 v29, v30, v30
	v_max_f32_e32 v23, v23, v29
	v_sub_f32_e32 v15, v15, v23
	v_sub_f32_e32 v17, v17, v23
	v_sub_f32_e32 v19, v19, v23
	v_sub_f32_e32 v21, v21, v23
	s_nop 1
	v_mov_b32_dpp v23, v4 quad_perm:[1,0,3,2] row_mask:0xf bank_mask:0xf
	s_waitcnt lgkmcnt(1)
	v_add_f32_e32 v37, v37, v38
	s_nop 1
	v_mov_b32_dpp v38, v37 row_half_mirror row_mask:0xf bank_mask:0xf
	v_exp_f32_e32 v15, v15
	v_exp_f32_e32 v17, v17
	s_waitcnt lgkmcnt(1)
	v_max_f32_e32 v23, v23, v23
	v_max_f32_e32 v4, v4, v23
	s_nop 1
	v_mov_b32_dpp v23, v4 quad_perm:[2,3,0,1] row_mask:0xf bank_mask:0xf
	s_waitcnt lgkmcnt(1)
	v_add_f32_e32 v32, v37, v38
	s_nop 1
	v_mov_b32_dpp v37, v32 row_mirror row_mask:0xf bank_mask:0xf
	v_div_fixup_f32 v22, v25, v22, 1.0
	v_exp_f32_e32 v19, v19
	s_waitcnt lgkmcnt(1)
	v_max_f32_e32 v23, v23, v23
	v_max_f32_e32 v4, v4, v23
	s_nop 1
	v_mov_b32_dpp v23, v4 row_half_mirror row_mask:0xf bank_mask:0xf
	s_waitcnt lgkmcnt(1)
	v_add_f32_e32 v25, v32, v37
	v_div_scale_f32 v29, s[6:7], v25, v25, 1.0
	v_exp_f32_e32 v21, v21
	s_waitcnt lgkmcnt(0)
	v_max_f32_e32 v23, v23, v23
	v_max_f32_e32 v4, v4, v23
	s_nop 1
	v_mov_b32_dpp v23, v4 row_mirror row_mask:0xf bank_mask:0xf
	v_rcp_f32_e32 v30, v29
	v_add_f32_e32 v32, 0, v15
	v_add_f32_e32 v24, v32, v17
	v_add_f32_e32 v24, v24, v19
	s_waitcnt lgkmcnt(0)
	v_max_f32_e32 v23, v23, v23
	v_max_f32_e32 v4, v4, v23
	v_add_f32_e32 v24, v24, v21
	v_sub_f32_e32 v23, v33, v4
	s_nop 1
	v_mov_b32_dpp v31, v24 quad_perm:[1,0,3,2] row_mask:0xf bank_mask:0xf
	v_fma_f32 v32, -v29, v30, 1.0
	v_exp_f32_e32 v23, v23
	v_sub_f32_e32 v33, v34, v4
	v_fmac_f32_e32 v30, v32, v30
	v_div_scale_f32 v32, vcc, 1.0, v25, 1.0
	v_exp_f32_e32 v33, v33
	v_sub_f32_e32 v34, v39, v4
	v_mul_f32_e32 v37, v32, v30
	v_exp_f32_e32 v34, v34
	v_sub_f32_e32 v4, v40, v4
	v_fma_f32 v38, -v29, v37, v32
	v_exp_f32_e32 v4, v4
	v_fmac_f32_e32 v37, v38, v30
	v_add_f32_e32 v38, 0, v23
	s_waitcnt lgkmcnt(0)
	v_add_f32_e32 v24, v24, v31
	v_add_f32_e32 v38, v38, v33
	s_nop 1
	v_mov_b32_dpp v31, v24 quad_perm:[2,3,0,1] row_mask:0xf bank_mask:0xf
	v_add_f32_e32 v38, v38, v34
	v_add_f32_e32 v38, v38, v4
	s_nop 1
	v_mov_b32_dpp v13, v38 quad_perm:[1,0,3,2] row_mask:0xf bank_mask:0xf
	v_fma_f32 v29, -v29, v37, v32
	s_waitcnt lgkmcnt(1)
	v_add_f32_e32 v24, v24, v31
	s_nop 1
	v_mov_b32_dpp v31, v24 row_half_mirror row_mask:0xf bank_mask:0xf
	v_div_fmas_f32 v29, v29, v30, v37
	s_waitcnt lgkmcnt(1)
	v_add_f32_e32 v13, v38, v13
	s_nop 1
	v_mov_b32_dpp v16, v13 quad_perm:[2,3,0,1] row_mask:0xf bank_mask:0xf
	v_div_fixup_f32 v25, v29, v25, 1.0
	s_waitcnt lgkmcnt(1)
	v_add_f32_e32 v24, v24, v31
	s_nop 1
	v_mov_b32_dpp v31, v24 row_mirror row_mask:0xf bank_mask:0xf
	v_cvt_f16_f32_e32 v12, v12
	s_waitcnt lgkmcnt(1)
	v_add_f32_e32 v13, v13, v16
	s_nop 1
	v_mov_b32_dpp v10, v13 row_half_mirror row_mask:0xf bank_mask:0xf
	v_cvt_f16_f32_e32 v26, v26
	s_waitcnt lgkmcnt(1)
	v_add_f32_e32 v24, v24, v31
	v_div_scale_f32 v30, s[6:7], v24, v24, 1.0
	v_rcp_f32_e32 v31, v30
	s_waitcnt lgkmcnt(0)
	v_add_f32_e32 v10, v13, v10
	s_nop 1
	v_mov_b32_dpp v11, v10 row_mirror row_mask:0xf bank_mask:0xf
	v_cvt_f16_f32_e32 v5, v5
	v_fma_f32 v16, -v30, v31, 1.0
	v_fmac_f32_e32 v31, v16, v31
	v_div_scale_f32 v16, vcc, 1.0, v24, 1.0
	v_mul_f32_e32 v13, v16, v31
	s_waitcnt lgkmcnt(0)
	v_add_f32_e32 v10, v10, v11
	v_fma_f32 v29, -v30, v13, v16
	v_div_scale_f32 v11, s[6:7], v10, v10, 1.0
	v_fmac_f32_e32 v13, v29, v31
	v_rcp_f32_e32 v29, v11
	v_fma_f32 v16, -v30, v13, v16
	v_div_fmas_f32 v13, v16, v31, v13
	v_div_fixup_f32 v13, v13, v24, 1.0
	v_fma_f32 v16, -v11, v29, 1.0
	v_fmac_f32_e32 v29, v16, v29
	s_movk_i32 s4, 0x1100
	v_mov_b32_e32 v16, 0x4800
	v_mad_u32_u24 v16, v1, s4, v16
	v_lshlrev_b32_e32 v24, 1, v8
	v_or_b32_e32 v30, v16, v24
	s_movk_i32 s4, 0x240
	v_mad_u32_u24 v31, v7, s4, v30
	s_waitcnt lgkmcnt(0)
	s_barrier
	ds_write_b16 v31, v14
	ds_write_b16 v31, v27 offset:32
	ds_write_b16 v31, v28 offset:64
	ds_write_b16 v31, v12 offset:96
	v_cvt_f16_f32_e32 v27, v35
	v_or_b32_e32 v12, 1, v9
	s_movk_i32 s4, 0x90
	v_cvt_f16_f32_e32 v28, v36
	v_mad_u32_u24 v14, v12, s4, v30
	ds_write_b16 v14, v26
	ds_write_b16 v14, v27 offset:32
	ds_write_b16 v14, v28 offset:64
	ds_write_b16 v14, v5 offset:96
	v_cvt_f16_f32_e32 v5, v15
	v_cvt_f16_f32_e32 v15, v17
	v_cvt_f16_f32_e32 v17, v19
	v_cvt_f16_f32_e32 v19, v21
	ds_write_b16 v14, v5 offset:144
	ds_write_b16 v14, v15 offset:176
	ds_write_b16 v14, v17 offset:208
	ds_write_b16 v14, v19 offset:240
	v_cvt_f16_f32_e32 v5, v23
	v_cvt_f16_f32_e32 v15, v33
	v_cvt_f16_f32_e32 v17, v34
	v_cvt_f16_f32_e32 v4, v4
	ds_write_b16 v14, v5 offset:288
	ds_write_b16 v14, v15 offset:320
	ds_write_b16 v14, v17 offset:352
	ds_write_b16 v14, v4 offset:384
	v_mul_u32_u24_e32 v4, 0x90, v8
	v_add3_u32 v4, v16, v4, v20
	s_waitcnt lgkmcnt(0)
	ds_read2_b64 v[36:39], v4 offset1:4
	ds_read2_b64 v[40:43], v4 offset0:8 offset1:12
	ds_read_b64_tr_b16 v[16:17], v0 offset:4608
	ds_read_b64_tr_b16 v[14:15], v0
	ds_read_b64_tr_b16 v[18:19], v0 offset:32
	ds_read_b64_tr_b16 v[30:31], v0 offset:64
	ds_read_b64_tr_b16 v[44:45], v0 offset:96
	ds_read_b64_tr_b16 v[20:21], v0 offset:4640
	ds_read_b64_tr_b16 v[32:33], v0 offset:4672
	ds_read_b64_tr_b16 v[46:47], v0 offset:4704
	s_waitcnt lgkmcnt(6)
	v_mfma_f32_16x16x32_f16 a[0:3], v[36:39], v[14:17], 0
	v_div_scale_f32 v4, vcc, 1.0, v10, 1.0
	v_mul_f32_e32 v5, v4, v29
	ds_read_b64_tr_b16 v[16:17], v0 offset:13824
	ds_read_b64_tr_b16 v[14:15], v0 offset:9216
	ds_read_b64_tr_b16 v[48:49], v0 offset:9248
	ds_read_b64_tr_b16 v[52:53], v0 offset:9280
	ds_read_b64_tr_b16 v[56:57], v0 offset:9312
	ds_read_b64_tr_b16 v[50:51], v0 offset:13856
	ds_read_b64_tr_b16 v[54:55], v0 offset:13888
	ds_read_b64_tr_b16 v[58:59], v0 offset:13920
	s_waitcnt lgkmcnt(6)
	v_mfma_f32_16x16x32_f16 a[0:3], v[40:43], v[14:17], a[0:3]
	v_fma_f32 v8, -v11, v5, v4
	v_fmac_f32_e32 v5, v8, v29
	v_fma_f32 v4, -v11, v5, v4
	v_mfma_f32_16x16x32_f16 a[4:7], v[36:39], v[18:21], 0
	v_div_fmas_f32 v4, v4, v29, v5
	v_div_fixup_f32 v4, v4, v10, 1.0
	s_movk_i32 s4, 0x1100
	v_mfma_f32_16x16x32_f16 a[8:11], v[36:39], v[30:33], 0
	v_accvgpr_read_b32 v5, a0
	v_accvgpr_read_b32 v8, a1
	v_accvgpr_read_b32 v9, a2
	s_waitcnt lgkmcnt(2)
	v_mfma_f32_16x16x32_f16 a[4:7], v[40:43], v[48:51], a[4:7]
	v_accvgpr_read_b32 v10, a3
	v_fma_mixlo_f16 v5, v5, v22, 0
	s_waitcnt lgkmcnt(1)
	v_mfma_f32_16x16x32_f16 a[0:3], v[40:43], v[52:55], a[8:11]
	v_mfma_f32_16x16x32_f16 a[8:11], v[36:39], v[44:47], 0
	ds_read_b64_tr_b16 v[28:29], v0 offset:4736
	ds_read_b64_tr_b16 v[26:27], v0 offset:128
	ds_read_b64_tr_b16 v[30:31], v0 offset:160
	ds_read_b64_tr_b16 v[44:45], v0 offset:192
	ds_read_b64_tr_b16 v[48:49], v0 offset:224
	ds_read_b64_tr_b16 v[32:33], v0 offset:4768
	ds_read_b64_tr_b16 v[46:47], v0 offset:4800
	ds_read_b64_tr_b16 v[50:51], v0 offset:4832
	v_accvgpr_read_b32 v11, a4
	v_accvgpr_read_b32 v14, a5
	v_accvgpr_read_b32 v15, a6
	v_accvgpr_read_b32 v16, a7
	v_accvgpr_read_b32 v17, a0
	v_accvgpr_read_b32 v18, a1
	s_waitcnt lgkmcnt(8)
	v_mfma_f32_16x16x32_f16 a[4:7], v[40:43], v[56:59], a[8:11]
	v_accvgpr_read_b32 v19, a3
	s_waitcnt lgkmcnt(6)
	v_mfma_f32_16x16x32_f16 a[8:11], v[36:39], v[26:29], 0
	ds_read_b64_tr_b16 v[28:29], v0 offset:13952
	ds_read_b64_tr_b16 v[26:27], v0 offset:9344
	ds_read_b64_tr_b16 v[52:53], v0 offset:9376
	ds_read_b64_tr_b16 v[56:57], v0 offset:9408
	ds_read_b64_tr_b16 v[60:61], v0 offset:9440
	ds_read_b64_tr_b16 v[54:55], v0 offset:13984
	ds_read_b64_tr_b16 v[58:59], v0 offset:14016
	ds_read_b64_tr_b16 v[62:63], v0 offset:14048
	v_accvgpr_read_b32 v0, a2
	v_accvgpr_read_b32 v20, a4
	s_waitcnt lgkmcnt(10)
	v_mfma_f32_16x16x32_f16 a[0:3], v[36:39], v[30:33], 0
	v_accvgpr_read_b32 v21, a5
	v_accvgpr_read_b32 v23, a6
	v_fma_mixlo_f16 v0, v0, v13, 0
	s_waitcnt lgkmcnt(2)
	v_mfma_f32_16x16x32_f16 a[0:3], v[40:43], v[52:55], a[0:3]
	v_mfma_f32_16x16x32_f16 a[8:11], v[40:43], v[26:29], a[8:11]
	v_accvgpr_read_b32 v26, a7
	v_mfma_f32_16x16x32_f16 a[4:7], v[36:39], v[44:47], 0
	s_nop 4
	v_accvgpr_read_b32 v31, a0
	v_accvgpr_read_b32 v32, a1
	v_accvgpr_read_b32 v33, a2
	v_accvgpr_read_b32 v34, a3
	v_mfma_f32_16x16x32_f16 a[0:3], v[36:39], v[48:51], 0
	v_accvgpr_read_b32 v27, a8
	v_accvgpr_read_b32 v28, a9
	v_accvgpr_read_b32 v29, a10
	s_waitcnt lgkmcnt(1)
	v_mfma_f32_16x16x32_f16 a[4:7], v[40:43], v[56:59], a[4:7]
	v_accvgpr_read_b32 v30, a11
	s_waitcnt lgkmcnt(0)
	v_mfma_f32_16x16x32_f16 a[0:3], v[40:43], v[60:63], a[0:3]
	v_mov_b32_e32 v43, 0x4800
	v_mad_u32_u24 v43, v1, s4, v43
	v_or_b32_e32 v1, v43, v24
	s_movk_i32 s4, 0x440
	v_mad_u32_u24 v24, v7, s4, v1
	ds_write_b16 v24, v5
	v_fma_mixlo_f16 v5, v8, v25, 0
	v_mad_u32_u24 v1, v12, s3, v1
	ds_write_b16 v1, v5
	v_fma_mixlo_f16 v5, v9, v13, 0
	ds_write_b16 v1, v5 offset:272
	v_fma_mixlo_f16 v5, v10, v4, 0
	ds_write_b16 v1, v5 offset:544
	v_fma_mixlo_f16 v5, v11, v22, 0
	ds_write_b16 v24, v5 offset:32
	v_fma_mixlo_f16 v5, v14, v25, 0
	ds_write_b16 v1, v5 offset:32
	v_fma_mixlo_f16 v5, v15, v13, 0
	ds_write_b16 v1, v5 offset:304
	v_fma_mixlo_f16 v5, v16, v4, 0
	ds_write_b16 v1, v5 offset:576
	v_fma_mixlo_f16 v5, v17, v22, 0
	ds_write_b16 v24, v5 offset:64
	ds_write_b16 v1, v0 offset:336
	v_fma_mixlo_f16 v0, v19, v4, 0
	v_fma_mixlo_f16 v5, v18, v25, 0
	ds_write_b16 v1, v0 offset:608
	v_fma_mixlo_f16 v0, v20, v22, 0
	ds_write_b16 v1, v5 offset:64
	ds_write_b16 v24, v0 offset:96
	v_fma_mixlo_f16 v0, v21, v25, 0
	ds_write_b16 v1, v0 offset:96
	v_fma_mixlo_f16 v0, v23, v13, 0
	ds_write_b16 v1, v0 offset:368
	v_fma_mixlo_f16 v0, v26, v4, 0
	ds_write_b16 v1, v0 offset:640
	v_fma_mixlo_f16 v0, v27, v22, 0
	ds_write_b16 v24, v0 offset:128
	v_fma_mixlo_f16 v0, v28, v25, 0
	ds_write_b16 v1, v0 offset:128
	v_fma_mixlo_f16 v0, v29, v13, 0
	ds_write_b16 v1, v0 offset:400
	v_fma_mixlo_f16 v0, v30, v4, 0
	ds_write_b16 v1, v0 offset:672
	v_fma_mixlo_f16 v0, v31, v22, 0
	ds_write_b16 v24, v0 offset:160
	v_fma_mixlo_f16 v0, v32, v25, 0
	ds_write_b16 v1, v0 offset:160
	v_fma_mixlo_f16 v0, v33, v13, 0
	v_accvgpr_read_b32 v35, a4
	ds_write_b16 v1, v0 offset:432
	v_fma_mixlo_f16 v0, v34, v4, 0
	v_accvgpr_read_b32 v36, a5
	ds_write_b16 v1, v0 offset:704
	v_fma_mixlo_f16 v0, v35, v22, 0
	v_accvgpr_read_b32 v37, a6
	ds_write_b16 v24, v0 offset:192
	v_fma_mixlo_f16 v0, v36, v25, 0
	v_accvgpr_read_b32 v38, a7
	ds_write_b16 v1, v0 offset:192
	v_fma_mixlo_f16 v0, v37, v13, 0
	v_accvgpr_read_b32 v39, a0
	ds_write_b16 v1, v0 offset:464
	v_fma_mixlo_f16 v0, v38, v4, 0
	v_accvgpr_read_b32 v40, a1
	ds_write_b16 v1, v0 offset:736
	v_fma_mixlo_f16 v0, v39, v22, 0
	v_accvgpr_read_b32 v41, a2
	ds_write_b16 v24, v0 offset:224
	v_fma_mixlo_f16 v0, v40, v25, 0
	v_accvgpr_read_b32 v42, a3
	ds_write_b16 v1, v0 offset:224
	v_fma_mixlo_f16 v0, v41, v13, 0
	ds_write_b16 v1, v0 offset:496
	v_fma_mixlo_f16 v0, v42, v4, 0
	ds_write_b16 v1, v0 offset:768
	v_lshl_or_b32 v4, s2, 6, v6
	s_movk_i32 s2, 0x600
	v_mov_b64_e32 v[0:1], s[8:9]
	v_mad_i64_i32 v[0:1], s[4:5], v4, s2, v[0:1]
	v_lshl_add_u64 v[0:1], v[0:1], 0, s[0:1]
	v_or_b32_e32 v4, v43, v2
	v_lshl_add_u64 v[0:1], v[0:1], 0, v[2:3]
	v_mul_u32_u24_e32 v2, 0x300, v7
	v_mad_u32_u24 v6, v7, s3, v4
	v_lshlrev_b32_e32 v2, 1, v2
	s_waitcnt lgkmcnt(0)
	ds_read_b128 v[8:11], v6
	v_lshl_add_u64 v[12:13], v[0:1], 0, v[2:3]
	ds_read_b128 v[0:3], v6 offset:1088
	s_movk_i32 s0, 0x1000
	v_add_co_u32_e32 v4, vcc, s0, v12
	s_waitcnt lgkmcnt(1)
	global_store_dwordx4 v[12:13], v[8:11], off nt
	v_addc_co_u32_e32 v5, vcc, 0, v13, vcc
	s_waitcnt lgkmcnt(0)
	global_store_dwordx4 v[4:5], v[0:3], off offset:2048 nt
	ds_read_b128 v[0:3], v6 offset:2176
	ds_read_b128 v[4:7], v6 offset:3264
	v_add_co_u32_e32 v8, vcc, 0x3000, v12
	s_nop 1
	v_addc_co_u32_e32 v9, vcc, 0, v13, vcc
	s_waitcnt lgkmcnt(1)
	global_store_dwordx4 v[8:9], v[0:3], off nt
	s_nop 1
	v_add_co_u32_e32 v0, vcc, 0x4000, v12
	s_nop 1
	v_addc_co_u32_e32 v1, vcc, 0, v13, vcc
	s_waitcnt lgkmcnt(0)
	global_store_dwordx4 v[0:1], v[4:7], off offset:2048 nt
	s_endpgm

	.amdhsa_kernel _Z6k_attnPKDF16_PKfPDF16_
		.amdhsa_group_segment_fixed_size 35840
		.amdhsa_private_segment_fixed_size 0
		.amdhsa_kernarg_size 24
		.amdhsa_user_sgpr_count 2
		.amdhsa_user_sgpr_dispatch_ptr 0
		.amdhsa_user_sgpr_queue_ptr 0
		.amdhsa_user_sgpr_kernarg_segment_ptr 1
		.amdhsa_user_sgpr_dispatch_id 0
		.amdhsa_user_sgpr_kernarg_preload_length 0
		.amdhsa_user_sgpr_kernarg_preload_offset 0
		.amdhsa_user_sgpr_private_segment_size 0
		.amdhsa_uses_dynamic_stack 0
		.amdhsa_enable_private_segment 0
		.amdhsa_system_sgpr_workgroup_id_x 1
		.amdhsa_system_sgpr_workgroup_id_y 0
		.amdhsa_system_sgpr_workgroup_id_z 0
		.amdhsa_system_sgpr_workgroup_info 0
		.amdhsa_system_vgpr_workitem_id 0
		.amdhsa_next_free_vgpr 84
		.amdhsa_next_free_sgpr 96
		.amdhsa_accum_offset 68
		.amdhsa_reserve_vcc 1
		.amdhsa_float_round_mode_32 0
		.amdhsa_float_round_mode_16_64 0
		.amdhsa_float_denorm_mode_32 3
		.amdhsa_float_denorm_mode_16_64 3
		.amdhsa_dx10_clamp 1
		.amdhsa_ieee_mode 1
		.amdhsa_fp16_overflow 0
		.amdhsa_tg_split 0
		.amdhsa_exception_fp_ieee_invalid_op 0
		.amdhsa_exception_fp_denorm_src 0
		.amdhsa_exception_fp_ieee_div_zero 0
		.amdhsa_exception_fp_ieee_overflow 0
		.amdhsa_exception_fp_ieee_underflow 0
		.amdhsa_exception_fp_ieee_inexact 0
		.amdhsa_exception_int_div_zero 0
	.end_amdhsa_kernel

amdhsa.kernels:
  - .agpr_count:     16
    .args:
      - .actual_access:  read_only
        .address_space:  global
        .offset:         0
        .size:           8
        .value_kind:     global_buffer
      - .actual_access:  read_only
        .address_space:  global
        .offset:         8
        .size:           8
        .value_kind:     global_buffer
      - .actual_access:  write_only
        .address_space:  global
        .offset:         16
        .size:           8
        .value_kind:     global_buffer
    .group_segment_fixed_size: 35840
    .kernarg_segment_align: 8
    .kernarg_segment_size: 24
    .language:       OpenCL C
    .language_version:
      - 2
      - 0
    .max_flat_workgroup_size: 256
    .name:           _Z6k_attnPKDF16_PKfPDF16_
    .private_segment_fixed_size: 0
    .sgpr_count:     16
    .sgpr_spill_count: 0
    .symbol:         _Z6k_attnPKDF16_PKfPDF16_.kd
    .uniform_work_group_size: 1
    .uses_dynamic_stack: false
    .vgpr_count:     84
    .vgpr_spill_count: 0
    .wavefront_size: 64
  - .agpr_count:     0
    .args:
      - .actual_access:  read_only
        .address_space:  global
        .offset:         0
        .size:           8
        .value_kind:     global_buffer
      - .actual_access:  read_only
        .address_space:  global
        .offset:         8
        .size:           8
        .value_kind:     global_buffer
      - .actual_access:  write_only
        .address_space:  global
        .offset:         16
        .size:           8
        .value_kind:     global_buffer
      - .actual_access:  write_only
        .address_space:  global
        .offset:         24
        .size:           8
        .value_kind:     global_buffer
      - .actual_access:  write_only
        .address_space:  global
        .offset:         32
        .size:           8
        .value_kind:     global_buffer
      - .actual_access:  write_only
        .address_space:  global
        .offset:         40
        .size:           8
        .value_kind:     global_buffer
    .group_segment_fixed_size: 0
    .kernarg_segment_align: 8
    .kernarg_segment_size: 48
    .language:       OpenCL C
    .language_version:
      - 2
      - 0
    .max_flat_workgroup_size: 256
    .name:           _Z11k_prep_miscPKiPKfPfPDv2_fS3_S3_
    .private_segment_fixed_size: 0
    .sgpr_count:     16
    .sgpr_spill_count: 0
    .symbol:         _Z11k_prep_miscPKiPKfPfPDv2_fS3_S3_.kd
    .uniform_work_group_size: 1
    .uses_dynamic_stack: false
    .vgpr_count:     6
    .vgpr_spill_count: 0
    .wavefront_size: 64
  - .agpr_count:     0
    .args:
      - .actual_access:  read_only
        .address_space:  global
        .offset:         0
        .size:           8
        .value_kind:     global_buffer
      - .actual_access:  write_only
        .address_space:  global
        .offset:         8
        .size:           8
        .value_kind:     global_buffer
    .group_segment_fixed_size: 0
    .kernarg_segment_align: 8
    .kernarg_segment_size: 16
    .language:       OpenCL C
    .language_version:
      - 2
      - 0
    .max_flat_workgroup_size: 256
    .name:           _Z7k_cvt_xPKfPDF16_
    .private_segment_fixed_size: 0
    .sgpr_count:     14
    .sgpr_spill_count: 0
    .symbol:         _Z7k_cvt_xPKfPDF16_.kd
    .uniform_work_group_size: 1
    .uses_dynamic_stack: false
    .vgpr_count:     12
    .vgpr_spill_count: 0
    .wavefront_size: 64
  - .agpr_count:     0
    .args:
      - .offset:         0
        .size:           176
        .value_kind:     by_value
    .group_segment_fixed_size: 9216
    .kernarg_segment_align: 8
    .kernarg_segment_size: 176
    .language:       OpenCL C
    .language_version:
      - 2
      - 0
    .max_flat_workgroup_size: 256
    .name:           _Z8k_wtrans8PrepArgs
    .private_segment_fixed_size: 0
    .sgpr_count:     44
    .sgpr_spill_count: 0
    .symbol:         _Z8k_wtrans8PrepArgs.kd
    .uniform_work_group_size: 1
    .uses_dynamic_stack: false
    .vgpr_count:     18
    .vgpr_spill_count: 0
    .wavefront_size: 64
  - .agpr_count:     0
    .args:
      - .offset:         0
        .size:           176
        .value_kind:     by_value
      - .actual_access:  read_only
        .address_space:  global
        .offset:         176
        .size:           8
        .value_kind:     global_buffer
      - .actual_access:  read_only
        .address_space:  global
        .offset:         184
        .size:           8
        .value_kind:     global_buffer
    .group_segment_fixed_size: 2048
    .kernarg_segment_align: 8
    .kernarg_segment_size: 192
    .language:       OpenCL C
    .language_version:
      - 2
      - 0
    .max_flat_workgroup_size: 256
    .name:           _Z8k_colvec8PrepArgsPKfS1_
    .private_segment_fixed_size: 0
    .sgpr_count:     38
    .sgpr_spill_count: 0
    .symbol:         _Z8k_colvec8PrepArgsPKfS1_.kd
    .uniform_work_group_size: 1
    .uses_dynamic_stack: false
    .vgpr_count:     114
    .vgpr_spill_count: 0
    .wavefront_size: 64
  - .agpr_count:     0
    .args:
      - .actual_access:  read_only
        .address_space:  global
        .offset:         0
        .size:           8
        .value_kind:     global_buffer
      - .actual_access:  write_only
        .address_space:  global
        .offset:         8
        .size:           8
        .value_kind:     global_buffer
    .group_segment_fixed_size: 0
    .kernarg_segment_align: 8
    .kernarg_segment_size: 16
    .language:       OpenCL C
    .language_version:
      - 2
      - 0
    .max_flat_workgroup_size: 256
    .name:           _Z9k_rowstatPKDv2_fPS_
    .private_segment_fixed_size: 0
    .sgpr_count:     16
    .sgpr_spill_count: 0
    .symbol:         _Z9k_rowstatPKDv2_fPS_.kd
    .uniform_work_group_size: 1
    .uses_dynamic_stack: false
    .vgpr_count:     28
    .vgpr_spill_count: 0
    .wavefront_size: 64
  - .agpr_count:     0
    .args:
      - .actual_access:  read_only
        .address_space:  global
        .offset:         0
        .size:           8
        .value_kind:     global_buffer
      - .actual_access:  read_only
        .address_space:  global
        .offset:         8
        .size:           8
        .value_kind:     global_buffer
      - .actual_access:  read_only
        .address_space:  global
        .offset:         16
        .size:           8
        .value_kind:     global_buffer
      - .actual_access:  read_only
        .address_space:  global
        .offset:         24
        .size:           8
        .value_kind:     global_buffer
      - .actual_access:  write_only
        .address_space:  global
        .offset:         32
        .size:           8
        .value_kind:     global_buffer
    .group_segment_fixed_size: 0
    .kernarg_segment_align: 8
    .kernarg_segment_size: 40
    .language:       OpenCL C
    .language_version:
      - 2
      - 0
    .max_flat_workgroup_size: 256
    .name:           _Z10k_final_lnPKDF16_PKDv2_fPKfS5_Pf
    .private_segment_fixed_size: 0
    .sgpr_count:     19
    .sgpr_spill_count: 0
    .symbol:         _Z10k_final_lnPKDF16_PKDv2_fPKfS5_Pf.kd
    .uniform_work_group_size: 1
    .uses_dynamic_stack: false
    .vgpr_count:     19
    .vgpr_spill_count: 0
    .wavefront_size: 64
  - .agpr_count:     0
    .args:
      - .offset:         0
        .size:           32
        .value_kind:     by_value
      - .offset:         32
        .size:           32
        .value_kind:     by_value
      - .offset:         64
        .size:           4
        .value_kind:     hidden_block_count_x
      - .offset:         68
        .size:           4
        .value_kind:     hidden_block_count_y
      - .offset:         72
        .size:           4
        .value_kind:     hidden_block_count_z
      - .offset:         76
        .size:           2
        .value_kind:     hidden_group_size_x
      - .offset:         78
        .size:           2
        .value_kind:     hidden_group_size_y
      - .offset:         80
        .size:           2
        .value_kind:     hidden_group_size_z
      - .offset:         82
        .size:           2
        .value_kind:     hidden_remainder_x
      - .offset:         84
        .size:           2
        .value_kind:     hidden_remainder_y
      - .offset:         86
        .size:           2
        .value_kind:     hidden_remainder_z
      - .offset:         104
        .size:           8
        .value_kind:     hidden_global_offset_x
      - .offset:         112
        .size:           8
        .value_kind:     hidden_global_offset_y
      - .offset:         120
        .size:           8
        .value_kind:     hidden_global_offset_z
      - .offset:         128
        .size:           2
        .value_kind:     hidden_grid_dims
      - .offset:         184
        .size:           4
        .value_kind:     hidden_dynamic_lds_size
    .group_segment_fixed_size: 0
    .kernarg_segment_align: 8
    .kernarg_segment_size: 320
    .language:       OpenCL C
    .language_version:
      - 2
      - 0
    .max_flat_workgroup_size: 512
    .name:           _Z6k_gemmIN2pg6EpiLinILi0EEELi768EEvNS0_4GemmET_
    .private_segment_fixed_size: 0
    .sgpr_count:     88
    .sgpr_spill_count: 0
    .symbol:         _Z6k_gemmIN2pg6EpiLinILi0EEELi768EEvNS0_4GemmET_.kd
    .uniform_work_group_size: 1
    .uses_dynamic_stack: false
    .vgpr_count:     254
    .vgpr_spill_count: 0
    .wavefront_size: 64
  - .agpr_count:     0
    .args:
      - .offset:         0
        .size:           32
        .value_kind:     by_value
      - .offset:         32
        .size:           56
        .value_kind:     by_value
      - .offset:         88
        .size:           4
        .value_kind:     hidden_block_count_x
      - .offset:         92
        .size:           4
        .value_kind:     hidden_block_count_y
      - .offset:         96
        .size:           4
        .value_kind:     hidden_block_count_z
      - .offset:         100
        .size:           2
        .value_kind:     hidden_group_size_x
      - .offset:         102
        .size:           2
        .value_kind:     hidden_group_size_y
      - .offset:         104
        .size:           2
        .value_kind:     hidden_group_size_z
      - .offset:         106
        .size:           2
        .value_kind:     hidden_remainder_x
      - .offset:         108
        .size:           2
        .value_kind:     hidden_remainder_y
      - .offset:         110
        .size:           2
        .value_kind:     hidden_remainder_z
      - .offset:         128
        .size:           8
        .value_kind:     hidden_global_offset_x
      - .offset:         136
        .size:           8
        .value_kind:     hidden_global_offset_y
      - .offset:         144
        .size:           8
        .value_kind:     hidden_global_offset_z
      - .offset:         152
        .size:           2
        .value_kind:     hidden_grid_dims
      - .offset:         208
        .size:           4
        .value_kind:     hidden_dynamic_lds_size
    .group_segment_fixed_size: 0
    .kernarg_segment_align: 8
    .kernarg_segment_size: 344
    .language:       OpenCL C
    .language_version:
      - 2
      - 0
    .max_flat_workgroup_size: 512
    .name:           _Z6k_gemmIN2pg6EpiResELi768EEvNS0_4GemmET_
    .private_segment_fixed_size: 0
    .sgpr_count:     108
    .sgpr_spill_count: 0
    .symbol:         _Z6k_gemmIN2pg6EpiResELi768EEvNS0_4GemmET_.kd
    .uniform_work_group_size: 1
    .uses_dynamic_stack: false
    .vgpr_count:     256
    .vgpr_spill_count: 0
    .wavefront_size: 64
  - .agpr_count:     0
    .args:
      - .offset:         0
        .size:           32
        .value_kind:     by_value
      - .offset:         32
        .size:           32
        .value_kind:     by_value
      - .offset:         64
        .size:           4
        .value_kind:     hidden_block_count_x
      - .offset:         68
        .size:           4
        .value_kind:     hidden_block_count_y
      - .offset:         72
        .size:           4
        .value_kind:     hidden_block_count_z
      - .offset:         76
        .size:           2
        .value_kind:     hidden_group_size_x
      - .offset:         78
        .size:           2
        .value_kind:     hidden_group_size_y
      - .offset:         80
        .size:           2
        .value_kind:     hidden_group_size_z
      - .offset:         82
        .size:           2
        .value_kind:     hidden_remainder_x
      - .offset:         84
        .size:           2
        .value_kind:     hidden_remainder_y
      - .offset:         86
        .size:           2
        .value_kind:     hidden_remainder_z
      - .offset:         104
        .size:           8
        .value_kind:     hidden_global_offset_x
      - .offset:         112
        .size:           8
        .value_kind:     hidden_global_offset_y
      - .offset:         120
        .size:           8
        .value_kind:     hidden_global_offset_z
      - .offset:         128
        .size:           2
        .value_kind:     hidden_grid_dims
      - .offset:         184
        .size:           4
        .value_kind:     hidden_dynamic_lds_size
    .group_segment_fixed_size: 0
    .kernarg_segment_align: 8
    .kernarg_segment_size: 320
    .language:       OpenCL C
    .language_version:
      - 2
      - 0
    .max_flat_workgroup_size: 512
    .name:           _Z6k_gemmIN2pg6EpiLinILi1EEELi768EEvNS0_4GemmET_
    .private_segment_fixed_size: 0
    .sgpr_count:     88
    .sgpr_spill_count: 0
    .symbol:         _Z6k_gemmIN2pg6EpiLinILi1EEELi768EEvNS0_4GemmET_.kd
    .uniform_work_group_size: 1
    .uses_dynamic_stack: false
    .vgpr_count:     254
    .vgpr_spill_count: 0
    .wavefront_size: 64
  - .agpr_count:     0
    .args:
      - .offset:         0
        .size:           32
        .value_kind:     by_value
      - .offset:         32
        .size:           56
        .value_kind:     by_value
      - .offset:         88
        .size:           4
        .value_kind:     hidden_block_count_x
      - .offset:         92
        .size:           4
        .value_kind:     hidden_block_count_y
      - .offset:         96
        .size:           4
        .value_kind:     hidden_block_count_z
      - .offset:         100
        .size:           2
        .value_kind:     hidden_group_size_x
      - .offset:         102
        .size:           2
        .value_kind:     hidden_group_size_y
      - .offset:         104
        .size:           2
        .value_kind:     hidden_group_size_z
      - .offset:         106
        .size:           2
        .value_kind:     hidden_remainder_x
      - .offset:         108
        .size:           2
        .value_kind:     hidden_remainder_y
      - .offset:         110
        .size:           2
        .value_kind:     hidden_remainder_z
      - .offset:         128
        .size:           8
        .value_kind:     hidden_global_offset_x
      - .offset:         136
        .size:           8
        .value_kind:     hidden_global_offset_y
      - .offset:         144
        .size:           8
        .value_kind:     hidden_global_offset_z
      - .offset:         152
        .size:           2
        .value_kind:     hidden_grid_dims
      - .offset:         208
        .size:           4
        .value_kind:     hidden_dynamic_lds_size
    .group_segment_fixed_size: 0
    .kernarg_segment_align: 8
    .kernarg_segment_size: 344
    .language:       OpenCL C
    .language_version:
      - 2
      - 0
    .max_flat_workgroup_size: 512
    .name:           _Z6k_gemmIN2pg6EpiResELi3072EEvNS0_4GemmET_
    .private_segment_fixed_size: 0
    .sgpr_count:     108
    .sgpr_spill_count: 0
    .symbol:         _Z6k_gemmIN2pg6EpiResELi3072EEvNS0_4GemmET_.kd
    .uniform_work_group_size: 1
    .uses_dynamic_stack: false
    .vgpr_count:     256
    .vgpr_spill_count: 0
    .wavefront_size: 64
